# cache-residency ordering: Q2 walks the MoE activation rows from the last (most recently written by MG1) to the first
# speedup vs baseline: 1.0042x; 1.0006x over previous
.LBB0_1945:
	v_readlane_b32 s4, v253, 57
	v_sub_u32_e32 v72, v1, v42
	v_add_u32_e32 v72, -1, v72
	v_ashrrev_i32_e32 v73, 31, v72
	v_readlane_b32 s5, v253, 58
	s_movk_i32 s3, 0x2c00
	v_lshlrev_b32_e32 v98, 1, v44
	v_lshl_add_u64 v[60:61], v[72:73], 2, s[4:5]
	global_load_dword v2, v[60:61], off
	v_readlane_b32 s4, v254, 13
	v_readlane_b32 s5, v254, 14
	v_mov_b32_e32 v53, v99
	v_mov_b32_e32 v55, v99
	v_mov_b32_e32 v57, v99
	v_mov_b32_e32 v59, v99
	s_waitcnt vmcnt(0)
	v_max_f32_e32 v2, v2, v2
	v_max_f32_e32 v43, 0x1e3ce508, v2
	v_mov_b64_e32 v[2:3], s[4:5]
	v_mad_i64_i32 v[2:3], s[4:5], v72, s3, v[2:3]
	v_lshl_add_u64 v[4:5], v[2:3], 0, v[98:99]
	global_load_dwordx4 v[64:67], v[4:5], off
	global_load_dwordx4 v[38:41], v[4:5], off offset:1024
	global_load_dwordx4 v[34:37], v[4:5], off offset:2048
	global_load_dwordx4 v[30:33], v[4:5], off offset:3072
	s_mov_b32 s3, 0x42fe0000
	v_lshl_add_u64 v[4:5], v[2:3], 0, v[52:53]
	v_div_scale_f32 v53, s[4:5], v43, v43, s3
	global_load_dwordx4 v[26:29], v[4:5], off
	v_lshl_add_u64 v[4:5], v[2:3], 0, v[54:55]
	v_rcp_f32_e32 v55, v53
	global_load_dwordx4 v[22:25], v[4:5], off
	v_lshl_add_u64 v[4:5], v[2:3], 0, v[56:57]
	global_load_dwordx4 v[18:21], v[4:5], off
	v_fma_f32 v57, -v53, v55, 1.0
	v_fmac_f32_e32 v55, v57, v55
	v_div_scale_f32 v57, vcc, s3, v43, s3
	v_lshl_add_u64 v[4:5], v[2:3], 0, v[58:59]
	v_mul_f32_e32 v59, v57, v55
	v_fma_f32 v62, -v53, v59, v57
	v_fmac_f32_e32 v59, v62, v55
	v_fma_f32 v53, -v53, v59, v57
	v_div_fmas_f32 v53, v53, v55, v59
	v_div_fixup_f32 v53, v53, v43, s3
	v_lshlrev_b32_e32 v98, 1, v46
	global_load_dwordx4 v[14:17], v[4:5], off
	v_lshl_add_u64 v[4:5], v[2:3], 0, v[98:99]
	v_lshlrev_b32_e32 v98, 1, v48
	v_mov_b64_e32 v[62:63], s[18:19]
	s_movk_i32 s3, 0x1600
	global_load_dwordx4 v[10:13], v[4:5], off
	v_lshl_add_u64 v[4:5], v[2:3], 0, v[98:99]
	v_lshlrev_b32_e32 v98, 1, v50
	v_mad_i64_i32 v[62:63], s[4:5], v72, s3, v[62:63]
	v_lshl_add_u64 v[2:3], v[2:3], 0, v[98:99]
	global_load_dwordx4 v[6:9], v[4:5], off
	s_waitcnt vmcnt(9)
	v_lshlrev_b32_e32 v55, 16, v64
	v_and_b32_e32 v57, 0xffff0000, v64
	v_lshlrev_b32_e32 v59, 16, v65
	v_and_b32_e32 v64, 0xffff0000, v65
	v_lshlrev_b32_e32 v65, 16, v66
	v_and_b32_e32 v66, 0xffff0000, v66
	v_mul_f32_e32 v66, v53, v66
	v_rndne_f32_e32 v66, v66
	v_cvt_i32_f32_e32 v66, v66
	v_mul_f32_e32 v57, v53, v57
	v_lshlrev_b32_e32 v68, 16, v67
	v_mul_f32_e32 v55, v53, v55
	v_rndne_f32_e32 v57, v57
	v_lshlrev_b32_e32 v66, 8, v66
	v_mul_f32_e32 v59, v53, v59
	v_mul_f32_e32 v64, v53, v64
	v_rndne_f32_e32 v55, v55
	v_cvt_i32_f32_e32 v57, v57
	v_and_b32_e32 v69, 0xff00, v66
	v_rndne_f32_e32 v59, v59
	v_mul_f32_e32 v66, v53, v68
	v_rndne_f32_e32 v64, v64
	v_cvt_i32_f32_e32 v55, v55
	v_cvt_i32_f32_sdwa v59, v59 dst_sel:WORD_1 dst_unused:UNUSED_PAD src0_sel:DWORD
	v_rndne_f32_e32 v66, v66
	v_cvt_i32_f32_e32 v64, v64
	v_cvt_i32_f32_sdwa v66, v66 dst_sel:WORD_1 dst_unused:UNUSED_PAD src0_sel:DWORD
	v_lshlrev_b32_e32 v57, 8, v57
	v_and_b32_e32 v67, 0xffff0000, v67
	v_and_b32_e32 v57, 0xff00, v57
	v_and_b32_e32 v59, 0xff0000, v59
	v_perm_b32 v55, v64, v55, s7
	v_mul_f32_e32 v65, v53, v65
	v_and_b32_e32 v68, 0xff0000, v66
	v_or3_b32 v66, v55, v57, v59
	v_mul_f32_e32 v55, v53, v67
	v_rndne_f32_e32 v65, v65
	v_rndne_f32_e32 v55, v55
	v_cvt_i32_f32_e32 v65, v65
	v_cvt_i32_f32_e32 v55, v55
	s_waitcnt vmcnt(8)
	v_lshlrev_b32_e32 v57, 16, v39
	v_and_b32_e32 v39, 0xffff0000, v39
	v_mul_f32_e32 v57, v53, v57
	v_perm_b32 v55, v55, v65, s7
	v_or3_b32 v67, v55, v69, v68
	v_lshlrev_b32_e32 v55, 16, v38
	v_and_b32_e32 v38, 0xffff0000, v38
	v_mul_f32_e32 v38, v53, v38
	v_mul_f32_e32 v55, v53, v55
	v_rndne_f32_e32 v38, v38
	v_mul_f32_e32 v39, v53, v39
	v_rndne_f32_e32 v55, v55
	v_cvt_i32_f32_e32 v38, v38
	v_rndne_f32_e32 v57, v57
	v_rndne_f32_e32 v39, v39
	v_cvt_i32_f32_e32 v55, v55
	v_cvt_i32_f32_sdwa v57, v57 dst_sel:WORD_1 dst_unused:UNUSED_PAD src0_sel:DWORD
	v_cvt_i32_f32_e32 v39, v39
	v_lshl_add_u64 v[64:65], v[62:63], 0, v[44:45]
	v_lshlrev_b32_e32 v59, 16, v40
	v_and_b32_e32 v40, 0xffff0000, v40
	v_lshlrev_b32_e32 v38, 8, v38
	global_load_dwordx4 v[2:5], v[2:3], off
	v_and_b32_e32 v38, 0xff00, v38
	global_store_dwordx2 v[64:65], v[66:67], off
	v_lshlrev_b32_e32 v66, 16, v41
	v_and_b32_e32 v41, 0xffff0000, v41
	v_mul_f32_e32 v40, v53, v40
	v_and_b32_e32 v57, 0xff0000, v57
	v_perm_b32 v39, v39, v55, s7
	v_mul_f32_e32 v59, v53, v59
	v_rndne_f32_e32 v40, v40
	v_mul_f32_e32 v66, v53, v66
	v_or3_b32 v38, v39, v38, v57
	v_mul_f32_e32 v39, v53, v41
	v_rndne_f32_e32 v59, v59
	v_cvt_i32_f32_e32 v40, v40
	v_rndne_f32_e32 v66, v66
	v_rndne_f32_e32 v39, v39
	v_cvt_i32_f32_e32 v59, v59
	v_cvt_i32_f32_sdwa v66, v66 dst_sel:WORD_1 dst_unused:UNUSED_PAD src0_sel:DWORD
	v_cvt_i32_f32_e32 v39, v39
	v_lshlrev_b32_e32 v40, 8, v40
	v_and_b32_e32 v40, 0xff00, v40
	v_and_b32_e32 v66, 0xff0000, v66
	v_perm_b32 v39, v39, v59, s7
	v_or3_b32 v39, v39, v40, v66
	global_store_dwordx2 v[64:65], v[38:39], off offset:512
	s_waitcnt vmcnt(10)
	v_lshlrev_b32_e32 v38, 16, v34
	v_and_b32_e32 v34, 0xffff0000, v34
	v_lshlrev_b32_e32 v39, 16, v35
	v_and_b32_e32 v35, 0xffff0000, v35
	v_mul_f32_e32 v34, v53, v34
	v_mul_f32_e32 v38, v53, v38
	v_rndne_f32_e32 v34, v34
	v_mul_f32_e32 v39, v53, v39
	v_mul_f32_e32 v35, v53, v35
	v_rndne_f32_e32 v38, v38
	v_cvt_i32_f32_e32 v34, v34
	v_rndne_f32_e32 v39, v39
	v_rndne_f32_e32 v35, v35
	v_cvt_i32_f32_e32 v38, v38
	v_cvt_i32_f32_sdwa v39, v39 dst_sel:WORD_1 dst_unused:UNUSED_PAD src0_sel:DWORD
	v_cvt_i32_f32_e32 v35, v35
	v_lshlrev_b32_e32 v40, 16, v36
	v_and_b32_e32 v36, 0xffff0000, v36
	v_lshlrev_b32_e32 v34, 8, v34
	v_lshlrev_b32_e32 v41, 16, v37
	v_and_b32_e32 v37, 0xffff0000, v37
	v_and_b32_e32 v34, 0xff00, v34
	v_mul_f32_e32 v36, v53, v36
	v_and_b32_e32 v39, 0xff0000, v39
	v_perm_b32 v35, v35, v38, s7
	v_mul_f32_e32 v40, v53, v40
	v_rndne_f32_e32 v36, v36
	v_mul_f32_e32 v41, v53, v41
	v_or3_b32 v34, v35, v34, v39
	v_mul_f32_e32 v35, v53, v37
	v_rndne_f32_e32 v40, v40
	v_cvt_i32_f32_e32 v36, v36
	v_rndne_f32_e32 v41, v41
	v_rndne_f32_e32 v35, v35
	v_cvt_i32_f32_e32 v40, v40
	v_cvt_i32_f32_sdwa v41, v41 dst_sel:WORD_1 dst_unused:UNUSED_PAD src0_sel:DWORD
	v_cvt_i32_f32_e32 v35, v35
	v_lshlrev_b32_e32 v36, 8, v36
	v_and_b32_e32 v36, 0xff00, v36
	v_and_b32_e32 v41, 0xff0000, v41
	v_perm_b32 v35, v35, v40, s7
	v_or3_b32 v35, v35, v36, v41
	global_store_dwordx2 v[64:65], v[34:35], off offset:1024
	s_waitcnt vmcnt(10)
	v_lshlrev_b32_e32 v34, 16, v30
	v_and_b32_e32 v30, 0xffff0000, v30
	v_lshlrev_b32_e32 v35, 16, v31
	v_and_b32_e32 v31, 0xffff0000, v31
	v_mul_f32_e32 v30, v53, v30
	v_mul_f32_e32 v34, v53, v34
	v_rndne_f32_e32 v30, v30
	v_mul_f32_e32 v35, v53, v35
	v_mul_f32_e32 v31, v53, v31
	v_rndne_f32_e32 v34, v34
	v_cvt_i32_f32_e32 v30, v30
	v_rndne_f32_e32 v35, v35
	v_rndne_f32_e32 v31, v31
	v_cvt_i32_f32_e32 v34, v34
	v_cvt_i32_f32_sdwa v35, v35 dst_sel:WORD_1 dst_unused:UNUSED_PAD src0_sel:DWORD
	v_cvt_i32_f32_e32 v31, v31
	v_lshlrev_b32_e32 v36, 16, v32
	v_and_b32_e32 v32, 0xffff0000, v32
	v_lshlrev_b32_e32 v30, 8, v30
	v_lshlrev_b32_e32 v37, 16, v33
	v_and_b32_e32 v33, 0xffff0000, v33
	v_and_b32_e32 v30, 0xff00, v30
	v_mul_f32_e32 v32, v53, v32
	v_and_b32_e32 v35, 0xff0000, v35
	v_perm_b32 v31, v31, v34, s7
	v_mul_f32_e32 v36, v53, v36
	v_rndne_f32_e32 v32, v32
	v_mul_f32_e32 v37, v53, v37
	v_or3_b32 v30, v31, v30, v35
	v_mul_f32_e32 v31, v53, v33
	v_rndne_f32_e32 v36, v36
	v_cvt_i32_f32_e32 v32, v32
	v_rndne_f32_e32 v37, v37
	v_rndne_f32_e32 v31, v31
	v_cvt_i32_f32_e32 v36, v36
	v_cvt_i32_f32_sdwa v37, v37 dst_sel:WORD_1 dst_unused:UNUSED_PAD src0_sel:DWORD
	v_cvt_i32_f32_e32 v31, v31
	v_lshlrev_b32_e32 v32, 8, v32
	v_and_b32_e32 v32, 0xff00, v32
	v_and_b32_e32 v37, 0xff0000, v37
	v_perm_b32 v31, v31, v36, s7
	v_or3_b32 v31, v31, v32, v37
	global_store_dwordx2 v[64:65], v[30:31], off offset:1536
	s_waitcnt vmcnt(10)
	v_lshlrev_b32_e32 v30, 16, v26
	v_and_b32_e32 v26, 0xffff0000, v26
	v_lshlrev_b32_e32 v31, 16, v27
	v_and_b32_e32 v27, 0xffff0000, v27
	v_mul_f32_e32 v26, v53, v26
	v_mul_f32_e32 v30, v53, v30
	v_rndne_f32_e32 v26, v26
	v_mul_f32_e32 v31, v53, v31
	v_mul_f32_e32 v27, v53, v27
	v_rndne_f32_e32 v30, v30
	v_cvt_i32_f32_e32 v26, v26
	v_rndne_f32_e32 v31, v31
	v_rndne_f32_e32 v27, v27
	v_cvt_i32_f32_e32 v30, v30
	v_cvt_i32_f32_sdwa v31, v31 dst_sel:WORD_1 dst_unused:UNUSED_PAD src0_sel:DWORD
	v_cvt_i32_f32_e32 v27, v27
	v_lshlrev_b32_e32 v32, 16, v28
	v_and_b32_e32 v28, 0xffff0000, v28
	v_lshlrev_b32_e32 v26, 8, v26
	v_lshlrev_b32_e32 v33, 16, v29
	v_and_b32_e32 v29, 0xffff0000, v29
	v_and_b32_e32 v26, 0xff00, v26
	v_mul_f32_e32 v28, v53, v28
	v_and_b32_e32 v31, 0xff0000, v31
	v_perm_b32 v27, v27, v30, s7
	v_mul_f32_e32 v32, v53, v32
	v_rndne_f32_e32 v28, v28
	v_mul_f32_e32 v33, v53, v33
	v_or3_b32 v26, v27, v26, v31
	v_mul_f32_e32 v27, v53, v29
	v_rndne_f32_e32 v32, v32
	v_cvt_i32_f32_e32 v28, v28
	v_rndne_f32_e32 v33, v33
	v_rndne_f32_e32 v27, v27
	v_cvt_i32_f32_e32 v32, v32
	v_cvt_i32_f32_sdwa v33, v33 dst_sel:WORD_1 dst_unused:UNUSED_PAD src0_sel:DWORD
	v_cvt_i32_f32_e32 v27, v27
	v_lshlrev_b32_e32 v28, 8, v28
	v_and_b32_e32 v28, 0xff00, v28
	v_and_b32_e32 v33, 0xff0000, v33
	v_perm_b32 v27, v27, v32, s7
	v_or3_b32 v27, v27, v28, v33
	global_store_dwordx2 v[64:65], v[26:27], off offset:2048
	s_waitcnt vmcnt(10)
	v_lshlrev_b32_e32 v26, 16, v22
	v_and_b32_e32 v22, 0xffff0000, v22
	v_lshlrev_b32_e32 v27, 16, v23
	v_and_b32_e32 v23, 0xffff0000, v23
	v_mul_f32_e32 v22, v53, v22
	v_mul_f32_e32 v26, v53, v26
	v_rndne_f32_e32 v22, v22
	v_mul_f32_e32 v27, v53, v27
	v_mul_f32_e32 v23, v53, v23
	v_rndne_f32_e32 v26, v26
	v_cvt_i32_f32_e32 v22, v22
	v_rndne_f32_e32 v27, v27
	v_rndne_f32_e32 v23, v23
	v_cvt_i32_f32_e32 v26, v26
	v_cvt_i32_f32_sdwa v27, v27 dst_sel:WORD_1 dst_unused:UNUSED_PAD src0_sel:DWORD
	v_cvt_i32_f32_e32 v23, v23
	v_lshlrev_b32_e32 v28, 16, v24
	v_and_b32_e32 v24, 0xffff0000, v24
	v_lshlrev_b32_e32 v22, 8, v22
	v_lshlrev_b32_e32 v29, 16, v25
	v_and_b32_e32 v25, 0xffff0000, v25
	v_and_b32_e32 v22, 0xff00, v22
	v_mul_f32_e32 v24, v53, v24
	v_and_b32_e32 v27, 0xff0000, v27
	v_perm_b32 v23, v23, v26, s7
	v_mul_f32_e32 v28, v53, v28
	v_rndne_f32_e32 v24, v24
	v_mul_f32_e32 v29, v53, v29
	v_or3_b32 v22, v23, v22, v27
	v_mul_f32_e32 v23, v53, v25
	v_rndne_f32_e32 v28, v28
	v_cvt_i32_f32_e32 v24, v24
	v_rndne_f32_e32 v29, v29
	v_rndne_f32_e32 v23, v23
	v_cvt_i32_f32_e32 v28, v28
	v_cvt_i32_f32_sdwa v29, v29 dst_sel:WORD_1 dst_unused:UNUSED_PAD src0_sel:DWORD
	v_cvt_i32_f32_e32 v23, v23
	v_lshlrev_b32_e32 v24, 8, v24
	v_and_b32_e32 v24, 0xff00, v24
	v_and_b32_e32 v29, 0xff0000, v29
	v_perm_b32 v23, v23, v28, s7
	v_or3_b32 v23, v23, v24, v29
	global_store_dwordx2 v[64:65], v[22:23], off offset:2560
	s_waitcnt vmcnt(10)
	v_lshlrev_b32_e32 v22, 16, v18
	v_and_b32_e32 v18, 0xffff0000, v18
	v_lshlrev_b32_e32 v23, 16, v19
	v_and_b32_e32 v19, 0xffff0000, v19
	v_mul_f32_e32 v18, v53, v18
	v_mul_f32_e32 v22, v53, v22
	v_rndne_f32_e32 v18, v18
	v_mul_f32_e32 v23, v53, v23
	v_mul_f32_e32 v19, v53, v19
	v_rndne_f32_e32 v22, v22
	v_cvt_i32_f32_e32 v18, v18
	v_rndne_f32_e32 v23, v23
	v_rndne_f32_e32 v19, v19
	v_cvt_i32_f32_e32 v22, v22
	v_cvt_i32_f32_sdwa v23, v23 dst_sel:WORD_1 dst_unused:UNUSED_PAD src0_sel:DWORD
	v_cvt_i32_f32_e32 v19, v19
	v_lshlrev_b32_e32 v24, 16, v20
	v_and_b32_e32 v20, 0xffff0000, v20
	v_lshlrev_b32_e32 v18, 8, v18
	v_lshlrev_b32_e32 v25, 16, v21
	v_and_b32_e32 v21, 0xffff0000, v21
	v_and_b32_e32 v18, 0xff00, v18
	v_mul_f32_e32 v20, v53, v20
	v_and_b32_e32 v23, 0xff0000, v23
	v_perm_b32 v19, v19, v22, s7
	v_mul_f32_e32 v24, v53, v24
	v_rndne_f32_e32 v20, v20
	v_mul_f32_e32 v25, v53, v25
	v_or3_b32 v18, v19, v18, v23
	v_mul_f32_e32 v19, v53, v21
	v_rndne_f32_e32 v24, v24
	v_cvt_i32_f32_e32 v20, v20
	v_rndne_f32_e32 v25, v25
	v_rndne_f32_e32 v19, v19
	v_cvt_i32_f32_e32 v24, v24
	v_cvt_i32_f32_sdwa v25, v25 dst_sel:WORD_1 dst_unused:UNUSED_PAD src0_sel:DWORD
	v_cvt_i32_f32_e32 v19, v19
	v_lshlrev_b32_e32 v20, 8, v20
	v_and_b32_e32 v20, 0xff00, v20
	v_and_b32_e32 v25, 0xff0000, v25
	v_perm_b32 v19, v19, v24, s7
	v_or3_b32 v19, v19, v20, v25
	global_store_dwordx2 v[64:65], v[18:19], off offset:3072
	s_waitcnt vmcnt(10)
	v_lshlrev_b32_e32 v18, 16, v14
	v_and_b32_e32 v14, 0xffff0000, v14
	v_lshlrev_b32_e32 v19, 16, v15
	v_and_b32_e32 v15, 0xffff0000, v15
	v_mul_f32_e32 v14, v53, v14
	v_mul_f32_e32 v18, v53, v18
	v_rndne_f32_e32 v14, v14
	v_mul_f32_e32 v19, v53, v19
	v_mul_f32_e32 v15, v53, v15
	v_rndne_f32_e32 v18, v18
	v_cvt_i32_f32_e32 v14, v14
	v_rndne_f32_e32 v19, v19
	v_rndne_f32_e32 v15, v15
	v_cvt_i32_f32_e32 v18, v18
	v_cvt_i32_f32_sdwa v19, v19 dst_sel:WORD_1 dst_unused:UNUSED_PAD src0_sel:DWORD
	v_cvt_i32_f32_e32 v15, v15
	v_lshlrev_b32_e32 v20, 16, v16
	v_and_b32_e32 v16, 0xffff0000, v16
	v_lshlrev_b32_e32 v14, 8, v14
	v_lshlrev_b32_e32 v21, 16, v17
	v_and_b32_e32 v17, 0xffff0000, v17
	v_and_b32_e32 v14, 0xff00, v14
	v_mul_f32_e32 v16, v53, v16
	v_and_b32_e32 v19, 0xff0000, v19
	v_perm_b32 v15, v15, v18, s7
	v_mul_f32_e32 v20, v53, v20
	v_rndne_f32_e32 v16, v16
	v_mul_f32_e32 v21, v53, v21
	v_or3_b32 v14, v15, v14, v19
	v_mul_f32_e32 v15, v53, v17
	v_rndne_f32_e32 v20, v20
	v_cvt_i32_f32_e32 v16, v16
	v_rndne_f32_e32 v21, v21
	v_rndne_f32_e32 v15, v15
	v_cvt_i32_f32_e32 v20, v20
	v_cvt_i32_f32_sdwa v21, v21 dst_sel:WORD_1 dst_unused:UNUSED_PAD src0_sel:DWORD
	v_cvt_i32_f32_e32 v15, v15
	v_lshlrev_b32_e32 v16, 8, v16
	v_and_b32_e32 v16, 0xff00, v16
	v_and_b32_e32 v21, 0xff0000, v21
	v_perm_b32 v15, v15, v20, s7
	v_or3_b32 v15, v15, v16, v21
	global_store_dwordx2 v[64:65], v[14:15], off offset:3584
	s_waitcnt vmcnt(10)
	v_lshlrev_b32_e32 v14, 16, v10
	v_and_b32_e32 v10, 0xffff0000, v10
	v_lshlrev_b32_e32 v15, 16, v11
	v_and_b32_e32 v11, 0xffff0000, v11
	v_mul_f32_e32 v10, v53, v10
	v_mul_f32_e32 v14, v53, v14
	v_rndne_f32_e32 v10, v10
	v_mul_f32_e32 v15, v53, v15
	v_mul_f32_e32 v11, v53, v11
	v_rndne_f32_e32 v14, v14
	v_cvt_i32_f32_e32 v10, v10
	v_rndne_f32_e32 v15, v15
	v_rndne_f32_e32 v11, v11
	v_cvt_i32_f32_e32 v14, v14
	v_cvt_i32_f32_sdwa v15, v15 dst_sel:WORD_1 dst_unused:UNUSED_PAD src0_sel:DWORD
	v_cvt_i32_f32_e32 v11, v11
	v_lshlrev_b32_e32 v16, 16, v12
	v_and_b32_e32 v12, 0xffff0000, v12
	v_lshlrev_b32_e32 v10, 8, v10
	v_lshlrev_b32_e32 v17, 16, v13
	v_and_b32_e32 v13, 0xffff0000, v13
	v_and_b32_e32 v10, 0xff00, v10
	v_mul_f32_e32 v12, v53, v12
	v_and_b32_e32 v15, 0xff0000, v15
	v_perm_b32 v11, v11, v14, s7
	v_mul_f32_e32 v16, v53, v16
	v_rndne_f32_e32 v12, v12
	v_mul_f32_e32 v17, v53, v17
	v_or3_b32 v10, v11, v10, v15
	v_mul_f32_e32 v11, v53, v13
	v_rndne_f32_e32 v16, v16
	v_cvt_i32_f32_e32 v12, v12
	v_rndne_f32_e32 v17, v17
	v_rndne_f32_e32 v11, v11
	v_cvt_i32_f32_e32 v16, v16
	v_cvt_i32_f32_sdwa v17, v17 dst_sel:WORD_1 dst_unused:UNUSED_PAD src0_sel:DWORD
	v_cvt_i32_f32_e32 v11, v11
	v_lshlrev_b32_e32 v12, 8, v12
	v_and_b32_e32 v12, 0xff00, v12
	v_and_b32_e32 v17, 0xff0000, v17
	v_perm_b32 v11, v11, v16, s7
	v_or3_b32 v11, v11, v12, v17
	v_lshl_add_u64 v[12:13], v[62:63], 0, v[46:47]
	global_store_dwordx2 v[12:13], v[10:11], off
	s_waitcnt vmcnt(10)
	v_lshlrev_b32_e32 v10, 16, v6
	v_and_b32_e32 v6, 0xffff0000, v6
	v_lshlrev_b32_e32 v11, 16, v7
	v_and_b32_e32 v7, 0xffff0000, v7
	v_mul_f32_e32 v6, v53, v6
	v_mul_f32_e32 v10, v53, v10
	v_rndne_f32_e32 v6, v6
	v_mul_f32_e32 v11, v53, v11
	v_mul_f32_e32 v7, v53, v7
	v_rndne_f32_e32 v10, v10
	v_cvt_i32_f32_e32 v6, v6
	v_rndne_f32_e32 v11, v11
	v_rndne_f32_e32 v7, v7
	v_cvt_i32_f32_e32 v10, v10
	v_cvt_i32_f32_sdwa v11, v11 dst_sel:WORD_1 dst_unused:UNUSED_PAD src0_sel:DWORD
	v_cvt_i32_f32_e32 v7, v7
	v_lshlrev_b32_e32 v12, 16, v8
	v_and_b32_e32 v8, 0xffff0000, v8
	v_lshlrev_b32_e32 v6, 8, v6
	v_lshlrev_b32_e32 v13, 16, v9
	v_and_b32_e32 v9, 0xffff0000, v9
	v_and_b32_e32 v6, 0xff00, v6
	v_mul_f32_e32 v8, v53, v8
	v_and_b32_e32 v11, 0xff0000, v11
	v_perm_b32 v7, v7, v10, s7
	v_mul_f32_e32 v12, v53, v12
	v_rndne_f32_e32 v8, v8
	v_mul_f32_e32 v13, v53, v13
	v_or3_b32 v6, v7, v6, v11
	v_mul_f32_e32 v7, v53, v9
	v_rndne_f32_e32 v12, v12
	v_cvt_i32_f32_e32 v8, v8
	v_rndne_f32_e32 v13, v13
	v_rndne_f32_e32 v7, v7
	v_cvt_i32_f32_e32 v12, v12
	v_cvt_i32_f32_sdwa v13, v13 dst_sel:WORD_1 dst_unused:UNUSED_PAD src0_sel:DWORD
	v_cvt_i32_f32_e32 v7, v7
	v_lshlrev_b32_e32 v8, 8, v8
	v_and_b32_e32 v8, 0xff00, v8
	v_and_b32_e32 v13, 0xff0000, v13
	v_perm_b32 v7, v7, v12, s7
	v_or3_b32 v7, v7, v8, v13
	v_lshl_add_u64 v[8:9], v[62:63], 0, v[48:49]
	global_store_dwordx2 v[8:9], v[6:7], off
	s_waitcnt vmcnt(10)
	v_lshlrev_b32_e32 v6, 16, v2
	v_and_b32_e32 v2, 0xffff0000, v2
	v_lshlrev_b32_e32 v7, 16, v3
	v_and_b32_e32 v3, 0xffff0000, v3
	v_mul_f32_e32 v2, v53, v2
	v_mul_f32_e32 v6, v53, v6
	v_rndne_f32_e32 v2, v2
	v_mul_f32_e32 v7, v53, v7
	v_mul_f32_e32 v3, v53, v3
	v_rndne_f32_e32 v6, v6
	v_cvt_i32_f32_e32 v2, v2
	v_rndne_f32_e32 v7, v7
	v_rndne_f32_e32 v3, v3
	v_cvt_i32_f32_e32 v6, v6
	v_cvt_i32_f32_sdwa v7, v7 dst_sel:WORD_1 dst_unused:UNUSED_PAD src0_sel:DWORD
	v_cvt_i32_f32_e32 v3, v3
	v_lshlrev_b32_e32 v8, 16, v4
	v_and_b32_e32 v4, 0xffff0000, v4
	v_lshlrev_b32_e32 v2, 8, v2
	v_lshlrev_b32_e32 v9, 16, v5
	v_and_b32_e32 v5, 0xffff0000, v5
	v_and_b32_e32 v2, 0xff00, v2
	v_mul_f32_e32 v4, v53, v4
	v_and_b32_e32 v7, 0xff0000, v7
	v_perm_b32 v3, v3, v6, s7
	v_mul_f32_e32 v8, v53, v8
	v_rndne_f32_e32 v4, v4
	v_mul_f32_e32 v9, v53, v9
	v_or3_b32 v2, v3, v2, v7
	v_mul_f32_e32 v3, v53, v5
	v_rndne_f32_e32 v8, v8
	v_cvt_i32_f32_e32 v4, v4
	v_rndne_f32_e32 v9, v9
	v_rndne_f32_e32 v3, v3
	v_cvt_i32_f32_e32 v8, v8
	v_cvt_i32_f32_sdwa v9, v9 dst_sel:WORD_1 dst_unused:UNUSED_PAD src0_sel:DWORD
	v_cvt_i32_f32_e32 v3, v3
	v_lshlrev_b32_e32 v4, 8, v4
	v_and_b32_e32 v4, 0xff00, v4
	v_and_b32_e32 v9, 0xff0000, v9
	v_perm_b32 v3, v3, v8, s7
	v_or3_b32 v3, v3, v4, v9
	v_lshl_add_u64 v[4:5], v[62:63], 0, v[50:51]
	global_store_dwordx2 v[4:5], v[2:3], off
	s_and_saveexec_b64 s[4:5], s[0:1]
	s_cbranch_execz .LBB0_1944
	v_mul_f32_e32 v2, 0x3c010204, v43
	global_store_dword v[60:61], v2, off
	s_branch .LBB0_1944
